# GEMM K-loops: all per-MMA-segment s_setprio 1/0 toggles removed (both wave halves stay at priority 0)
# speedup vs baseline: 1.0044x; 1.0044x over previous
.LBB0_123:
	s_mov_b32 s61, 0
	s_waitcnt lgkmcnt(0)
	v_mov_b32_e32 v201, v199
	v_lshl_add_u64 v[208:209], s[42:43], 0, v[198:199]
	v_lshl_add_u64 v[210:211], s[42:43], 0, v[200:201]
	s_barrier
	s_cmp_eq_u32 s60, -2
	s_cbranch_scc1 .Lnz_P1b_first
	s_waitcnt lgkmcnt(0)
	v_mfma_f32_16x16x128_f8f6f4 v[126:129], v[18:25], v[58:65], v[126:129]
	v_mfma_f32_16x16x128_f8f6f4 v[122:125], v[26:33], v[58:65], v[122:125]
	v_mfma_f32_16x16x128_f8f6f4 v[110:113], v[18:25], v[50:57], v[110:113]
	v_mfma_f32_16x16x128_f8f6f4 v[106:109], v[26:33], v[50:57], v[106:109]
	v_mfma_f32_16x16x128_f8f6f4 v[78:81], v[18:25], v[42:49], v[78:81]
	v_mfma_f32_16x16x128_f8f6f4 v[74:77], v[26:33], v[42:49], v[74:77]
	v_mfma_f32_16x16x128_f8f6f4 v[70:73], v[18:25], v[34:41], v[70:73]
	v_mfma_f32_16x16x128_f8f6f4 v[66:69], v[26:33], v[34:41], v[66:69]
	v_mfma_f32_16x16x128_f8f6f4 v[118:121], v[2:9], v[58:65], v[118:121]
	v_mfma_f32_16x16x128_f8f6f4 v[114:117], v[10:17], v[58:65], v[114:117]
	v_mfma_f32_16x16x128_f8f6f4 v[94:97], v[2:9], v[50:57], v[94:97]
	v_mfma_f32_16x16x128_f8f6f4 v[90:93], v[10:17], v[50:57], v[90:93]
	v_mfma_f32_16x16x128_f8f6f4 v[98:101], v[2:9], v[42:49], v[98:101]
	v_mfma_f32_16x16x128_f8f6f4 v[102:105], v[10:17], v[42:49], v[102:105]
	v_mfma_f32_16x16x128_f8f6f4 v[82:85], v[2:9], v[34:41], v[82:85]
	v_mfma_f32_16x16x128_f8f6f4 v[86:89], v[10:17], v[34:41], v[86:89]
.Lnz_P1b_back:
	s_barrier
	s_add_i32 s46, 0, 0x18000
	s_add_i32 s47, 0, 0x1c000
	v_add_u32_e32 v14, s46, v217
	v_add_u32_e32 v30, s47, v217
	ds_read_b128 v[2:5], v14
	ds_read_b128 v[6:9], v14 offset:16
	ds_read_b128 v[10:13], v14 offset:2048
	ds_read_b128 v[14:17], v14 offset:2064
	ds_read_b128 v[18:21], v30
	ds_read_b128 v[22:25], v30 offset:16
	ds_read_b128 v[26:29], v30 offset:2048
	ds_read_b128 v[30:33], v30 offset:2064
	s_mov_b32 m0, s83
	ds_read_b128 v[34:37], v220 offset:32768
	ds_read_b128 v[38:41], v220 offset:32784
	ds_read_b128 v[42:45], v220 offset:34816
	ds_read_b128 v[46:49], v220 offset:34832
	ds_read_b128 v[50:53], v220 offset:36864
	ds_read_b128 v[54:57], v220 offset:36880
	ds_read_b128 v[58:61], v220 offset:38912
	ds_read_b128 v[62:65], v220 offset:38928
	global_load_lds_dwordx4 v213, s[42:43]
	s_mov_b32 m0, s84
	s_nop 0
	global_load_lds_dwordx4 v214, s[42:43]
	s_waitcnt vmcnt(8)
	s_waitcnt lgkmcnt(0)
	s_barrier
	s_waitcnt lgkmcnt(0)
	v_mfma_f32_16x16x128_f8f6f4 v[190:193], v[2:9], v[34:41], v[190:193]
	v_mfma_f32_16x16x128_f8f6f4 v[186:189], v[10:17], v[34:41], v[186:189]
	v_mfma_f32_16x16x128_f8f6f4 v[174:177], v[2:9], v[42:49], v[174:177]
	v_mfma_f32_16x16x128_f8f6f4 v[170:173], v[10:17], v[42:49], v[170:173]
	v_mfma_f32_16x16x128_f8f6f4 v[158:161], v[2:9], v[50:57], v[158:161]
	v_mfma_f32_16x16x128_f8f6f4 v[154:157], v[10:17], v[50:57], v[154:157]
	v_mfma_f32_16x16x128_f8f6f4 v[142:145], v[2:9], v[58:65], v[142:145]
	v_mfma_f32_16x16x128_f8f6f4 v[138:141], v[10:17], v[58:65], v[138:141]
	v_mfma_f32_16x16x128_f8f6f4 v[182:185], v[18:25], v[34:41], v[182:185]
	v_mfma_f32_16x16x128_f8f6f4 v[178:181], v[26:33], v[34:41], v[178:181]
	v_mfma_f32_16x16x128_f8f6f4 v[166:169], v[18:25], v[42:49], v[166:169]
	v_mfma_f32_16x16x128_f8f6f4 v[162:165], v[26:33], v[42:49], v[162:165]
	v_mfma_f32_16x16x128_f8f6f4 v[150:153], v[18:25], v[50:57], v[150:153]
	v_mfma_f32_16x16x128_f8f6f4 v[146:149], v[26:33], v[50:57], v[146:149]
	v_mfma_f32_16x16x128_f8f6f4 v[134:137], v[18:25], v[58:65], v[134:137]
	v_mfma_f32_16x16x128_f8f6f4 v[130:133], v[26:33], v[58:65], v[130:133]
	s_barrier
	s_add_i32 s42, s46, s55
	v_lshl_add_u64 v[206:207], v[206:207], 0, s[30:31]
	s_mov_b32 m0, s42
	ds_read_b128 v[34:37], v220 offset:49152
	ds_read_b128 v[38:41], v220 offset:49168
	ds_read_b128 v[42:45], v220 offset:51200
	ds_read_b128 v[46:49], v220 offset:51216
	ds_read_b128 v[50:53], v220 offset:53248
	ds_read_b128 v[54:57], v220 offset:53264
	ds_read_b128 v[58:61], v220 offset:55296
	ds_read_b128 v[62:65], v220 offset:55312
	global_load_lds_dwordx4 v[206:207], off
	s_add_i32 m0, s42, 0x2000
	s_add_u32 s40, s40, 0x8080
	v_lshl_add_u64 v[204:205], v[204:205], 0, s[30:31]
	s_addc_u32 s41, s41, 0
	s_add_i32 s42, s47, s55
	global_load_lds_dwordx4 v[204:205], off
	v_lshl_add_u64 v[204:205], s[40:41], 0, v[194:195]
	s_mov_b32 m0, s42
	s_nop 0
	global_load_lds_dwordx4 v[204:205], off
	v_lshl_add_u64 v[204:205], s[40:41], 0, v[196:197]
	s_add_i32 m0, s42, 0x2000
	s_nop 0
	global_load_lds_dwordx4 v[204:205], off
	v_lshl_add_u64 v[204:205], v[208:209], 0, s[30:31]
	s_mov_b32 m0, s86
	s_nop 0
	global_load_lds_dwordx4 v[204:205], off
	v_lshl_add_u64 v[204:205], v[210:211], 0, s[30:31]
	s_mov_b32 m0, s87
	s_nop 0
	global_load_lds_dwordx4 v[204:205], off
	s_waitcnt vmcnt(8)
	s_waitcnt lgkmcnt(0)
	s_barrier
	s_waitcnt lgkmcnt(0)
	v_mfma_f32_16x16x128_f8f6f4 v[126:129], v[2:9], v[34:41], v[126:129]
	v_mfma_f32_16x16x128_f8f6f4 v[122:125], v[10:17], v[34:41], v[122:125]
	v_mfma_f32_16x16x128_f8f6f4 v[110:113], v[2:9], v[42:49], v[110:113]
	v_mfma_f32_16x16x128_f8f6f4 v[106:109], v[10:17], v[42:49], v[106:109]
	v_mfma_f32_16x16x128_f8f6f4 v[78:81], v[2:9], v[50:57], v[78:81]
	v_mfma_f32_16x16x128_f8f6f4 v[74:77], v[10:17], v[50:57], v[74:77]
	v_mfma_f32_16x16x128_f8f6f4 v[70:73], v[2:9], v[58:65], v[70:73]
	v_mfma_f32_16x16x128_f8f6f4 v[66:69], v[10:17], v[58:65], v[66:69]
	v_mfma_f32_16x16x128_f8f6f4 v[118:121], v[18:25], v[34:41], v[118:121]
	v_mfma_f32_16x16x128_f8f6f4 v[114:117], v[26:33], v[34:41], v[114:117]
	v_mfma_f32_16x16x128_f8f6f4 v[94:97], v[18:25], v[42:49], v[94:97]
	v_mfma_f32_16x16x128_f8f6f4 v[90:93], v[26:33], v[42:49], v[90:93]
	v_mfma_f32_16x16x128_f8f6f4 v[98:101], v[18:25], v[50:57], v[98:101]
	v_mfma_f32_16x16x128_f8f6f4 v[102:105], v[26:33], v[50:57], v[102:105]
	v_mfma_f32_16x16x128_f8f6f4 v[82:85], v[18:25], v[58:65], v[82:85]
	v_mfma_f32_16x16x128_f8f6f4 v[86:89], v[26:33], v[58:65], v[86:89]
	s_barrier
	s_add_i32 s60, s60, 2
	s_add_u32 s62, s62, 0x100
	s_addc_u32 s63, s63, 0
	s_add_u32 s56, s56, 0x100
	s_addc_u32 s57, s57, 0
	s_cmp_gt_u32 s60, 5
	s_cbranch_scc1 .LBB0_130

.LBB0_128:
	s_add_u32 s42, s62, 0x80
	s_addc_u32 s43, s63, 0
	s_waitcnt lgkmcnt(0)
	s_and_b64 s[40:41], s[40:41], exec
	s_cselect_b32 s43, s9, s43
	s_cselect_b32 s42, s8, s42
	s_cselect_b32 s41, s2, s57
	s_cselect_b32 s40, s7, s56
	s_barrier
	s_cmp_eq_u32 s60, -2
	s_cbranch_scc1 .Lnz_P1a_first
	s_waitcnt lgkmcnt(0)
	v_mfma_f32_16x16x128_f8f6f4 v[190:193], v[18:25], v[58:65], v[190:193]
	v_mfma_f32_16x16x128_f8f6f4 v[186:189], v[26:33], v[58:65], v[186:189]
	v_mfma_f32_16x16x128_f8f6f4 v[174:177], v[18:25], v[50:57], v[174:177]
	v_mfma_f32_16x16x128_f8f6f4 v[170:173], v[26:33], v[50:57], v[170:173]
	v_mfma_f32_16x16x128_f8f6f4 v[158:161], v[18:25], v[42:49], v[158:161]
	v_mfma_f32_16x16x128_f8f6f4 v[154:157], v[26:33], v[42:49], v[154:157]
	v_mfma_f32_16x16x128_f8f6f4 v[142:145], v[18:25], v[34:41], v[142:145]
	v_mfma_f32_16x16x128_f8f6f4 v[138:141], v[26:33], v[34:41], v[138:141]
	v_mfma_f32_16x16x128_f8f6f4 v[182:185], v[2:9], v[58:65], v[182:185]
	v_mfma_f32_16x16x128_f8f6f4 v[178:181], v[10:17], v[58:65], v[178:181]
	v_mfma_f32_16x16x128_f8f6f4 v[166:169], v[2:9], v[50:57], v[166:169]
	v_mfma_f32_16x16x128_f8f6f4 v[162:165], v[10:17], v[50:57], v[162:165]
	v_mfma_f32_16x16x128_f8f6f4 v[150:153], v[2:9], v[42:49], v[150:153]
	v_mfma_f32_16x16x128_f8f6f4 v[146:149], v[10:17], v[42:49], v[146:149]
	v_mfma_f32_16x16x128_f8f6f4 v[134:137], v[2:9], v[34:41], v[134:137]
	v_mfma_f32_16x16x128_f8f6f4 v[130:133], v[10:17], v[34:41], v[130:133]

.LBB0_482:
	s_mov_b32 s71, 0
	s_waitcnt lgkmcnt(0)
	v_mov_b32_e32 v201, v199
	v_lshl_add_u64 v[224:225], s[36:37], 0, v[198:199]
	v_lshl_add_u64 v[226:227], s[36:37], 0, v[200:201]
	s_barrier
	s_waitcnt lgkmcnt(0)
	v_mfma_f32_16x16x128_f8f6f4 v[126:129], v[18:25], v[58:65], v[126:129]
	v_mfma_f32_16x16x128_f8f6f4 v[122:125], v[26:33], v[58:65], v[122:125]
	v_mfma_f32_16x16x128_f8f6f4 v[110:113], v[18:25], v[50:57], v[110:113]
	v_mfma_f32_16x16x128_f8f6f4 v[106:109], v[26:33], v[50:57], v[106:109]
	v_mfma_f32_16x16x128_f8f6f4 v[86:89], v[18:25], v[42:49], v[86:89]
	v_mfma_f32_16x16x128_f8f6f4 v[82:85], v[26:33], v[42:49], v[82:85]
	v_mfma_f32_16x16x128_f8f6f4 v[70:73], v[18:25], v[34:41], v[70:73]
	v_mfma_f32_16x16x128_f8f6f4 v[66:69], v[26:33], v[34:41], v[66:69]
	v_mfma_f32_16x16x128_f8f6f4 v[118:121], v[2:9], v[58:65], v[118:121]
	v_mfma_f32_16x16x128_f8f6f4 v[114:117], v[10:17], v[58:65], v[114:117]
	v_mfma_f32_16x16x128_f8f6f4 v[102:105], v[2:9], v[50:57], v[102:105]
	v_mfma_f32_16x16x128_f8f6f4 v[98:101], v[10:17], v[50:57], v[98:101]
	v_mfma_f32_16x16x128_f8f6f4 v[94:97], v[2:9], v[42:49], v[94:97]
	v_mfma_f32_16x16x128_f8f6f4 v[90:93], v[10:17], v[42:49], v[90:93]
	v_mfma_f32_16x16x128_f8f6f4 v[78:81], v[2:9], v[34:41], v[78:81]
	v_mfma_f32_16x16x128_f8f6f4 v[74:77], v[10:17], v[34:41], v[74:77]
	s_barrier
	s_add_i32 s2, 0, 0x18000
	s_add_i32 s38, 0, 0x1c000
	v_add_u32_e32 v14, s2, v219
	v_add_u32_e32 v30, s38, v219
	ds_read_b128 v[2:5], v14
	ds_read_b128 v[6:9], v14 offset:16
	ds_read_b128 v[10:13], v14 offset:2048
	ds_read_b128 v[14:17], v14 offset:2064
	ds_read_b128 v[18:21], v30
	ds_read_b128 v[22:25], v30 offset:16
	ds_read_b128 v[26:29], v30 offset:2048
	ds_read_b128 v[30:33], v30 offset:2064
	s_mov_b32 m0, s51
	ds_read_b128 v[34:37], v222 offset:32768
	ds_read_b128 v[38:41], v222 offset:32784
	ds_read_b128 v[42:45], v222 offset:34816
	ds_read_b128 v[46:49], v222 offset:34832
	ds_read_b128 v[50:53], v222 offset:36864
	ds_read_b128 v[54:57], v222 offset:36880
	ds_read_b128 v[58:61], v222 offset:38912
	ds_read_b128 v[62:65], v222 offset:38928
	global_load_lds_dwordx4 v215, s[36:37]
	s_mov_b32 m0, s53
	s_nop 0
	global_load_lds_dwordx4 v216, s[36:37]
	s_waitcnt vmcnt(8)
	s_waitcnt lgkmcnt(0)
	s_barrier
	s_waitcnt lgkmcnt(0)
	v_mfma_f32_16x16x128_f8f6f4 v[190:193], v[2:9], v[34:41], v[190:193]
	v_mfma_f32_16x16x128_f8f6f4 v[186:189], v[10:17], v[34:41], v[186:189]
	v_mfma_f32_16x16x128_f8f6f4 v[174:177], v[2:9], v[42:49], v[174:177]
	v_mfma_f32_16x16x128_f8f6f4 v[170:173], v[10:17], v[42:49], v[170:173]
	v_mfma_f32_16x16x128_f8f6f4 v[158:161], v[2:9], v[50:57], v[158:161]
	v_mfma_f32_16x16x128_f8f6f4 v[154:157], v[10:17], v[50:57], v[154:157]
	v_mfma_f32_16x16x128_f8f6f4 v[142:145], v[2:9], v[58:65], v[142:145]
	v_mfma_f32_16x16x128_f8f6f4 v[138:141], v[10:17], v[58:65], v[138:141]
	v_mfma_f32_16x16x128_f8f6f4 v[182:185], v[18:25], v[34:41], v[182:185]
	v_mfma_f32_16x16x128_f8f6f4 v[178:181], v[26:33], v[34:41], v[178:181]
	v_mfma_f32_16x16x128_f8f6f4 v[166:169], v[18:25], v[42:49], v[166:169]
	v_mfma_f32_16x16x128_f8f6f4 v[162:165], v[26:33], v[42:49], v[162:165]
	v_mfma_f32_16x16x128_f8f6f4 v[150:153], v[18:25], v[50:57], v[150:153]
	v_mfma_f32_16x16x128_f8f6f4 v[146:149], v[26:33], v[50:57], v[146:149]
	v_mfma_f32_16x16x128_f8f6f4 v[134:137], v[18:25], v[58:65], v[134:137]
	v_mfma_f32_16x16x128_f8f6f4 v[130:133], v[26:33], v[58:65], v[130:133]
	s_barrier
	s_add_i32 s2, s2, s42
	v_lshl_add_u64 v[212:213], v[212:213], 0, s[18:19]
	s_mov_b32 m0, s2
	ds_read_b128 v[34:37], v222 offset:49152
	ds_read_b128 v[38:41], v222 offset:49168
	ds_read_b128 v[42:45], v222 offset:51200
	ds_read_b128 v[46:49], v222 offset:51216
	ds_read_b128 v[50:53], v222 offset:53248
	ds_read_b128 v[54:57], v222 offset:53264
	ds_read_b128 v[58:61], v222 offset:55296
	ds_read_b128 v[62:65], v222 offset:55312
	global_load_lds_dwordx4 v[212:213], off
	s_add_i32 m0, s2, 0x2000
	s_add_u32 s2, s34, 0xa080
	v_lshl_add_u64 v[210:211], v[210:211], 0, s[18:19]
	s_addc_u32 s3, s35, 0
	s_add_i32 s34, s38, s42
	global_load_lds_dwordx4 v[210:211], off
	v_lshl_add_u64 v[210:211], s[2:3], 0, v[194:195]
	s_mov_b32 m0, s34
	s_nop 0
	global_load_lds_dwordx4 v[210:211], off
	v_lshl_add_u64 v[210:211], s[2:3], 0, v[196:197]
	s_add_i32 m0, s34, 0x2000
	s_nop 0
	global_load_lds_dwordx4 v[210:211], off
	v_lshl_add_u64 v[210:211], v[224:225], 0, s[18:19]
	s_mov_b32 m0, s60
	s_nop 0
	global_load_lds_dwordx4 v[210:211], off
	v_lshl_add_u64 v[210:211], v[226:227], 0, s[18:19]
	s_mov_b32 m0, s61
	s_nop 0
	global_load_lds_dwordx4 v[210:211], off
	s_waitcnt vmcnt(8)
	s_waitcnt lgkmcnt(0)
	s_barrier
	s_waitcnt lgkmcnt(0)
	v_mfma_f32_16x16x128_f8f6f4 v[126:129], v[2:9], v[34:41], v[126:129]
	v_mfma_f32_16x16x128_f8f6f4 v[122:125], v[10:17], v[34:41], v[122:125]
	v_mfma_f32_16x16x128_f8f6f4 v[110:113], v[2:9], v[42:49], v[110:113]
	v_mfma_f32_16x16x128_f8f6f4 v[106:109], v[10:17], v[42:49], v[106:109]
	v_mfma_f32_16x16x128_f8f6f4 v[86:89], v[2:9], v[50:57], v[86:89]
	v_mfma_f32_16x16x128_f8f6f4 v[82:85], v[10:17], v[50:57], v[82:85]
	v_mfma_f32_16x16x128_f8f6f4 v[70:73], v[2:9], v[58:65], v[70:73]
	v_mfma_f32_16x16x128_f8f6f4 v[66:69], v[10:17], v[58:65], v[66:69]
	v_mfma_f32_16x16x128_f8f6f4 v[118:121], v[18:25], v[34:41], v[118:121]
	v_mfma_f32_16x16x128_f8f6f4 v[114:117], v[26:33], v[34:41], v[114:117]
	v_mfma_f32_16x16x128_f8f6f4 v[102:105], v[18:25], v[42:49], v[102:105]
	v_mfma_f32_16x16x128_f8f6f4 v[98:101], v[26:33], v[42:49], v[98:101]
	v_mfma_f32_16x16x128_f8f6f4 v[94:97], v[18:25], v[50:57], v[94:97]
	v_mfma_f32_16x16x128_f8f6f4 v[90:93], v[26:33], v[50:57], v[90:93]
	v_mfma_f32_16x16x128_f8f6f4 v[78:81], v[18:25], v[58:65], v[78:81]
	v_mfma_f32_16x16x128_f8f6f4 v[74:77], v[26:33], v[58:65], v[74:77]
	s_barrier
	s_add_i32 s70, s70, 2
	s_add_u32 s30, s30, 0x100
	s_addc_u32 s31, s31, 0
	s_add_u32 s68, s68, 0x100
	s_addc_u32 s69, s69, 0
	s_cmp_gt_u32 s70, 7
	s_cbranch_scc1 .LBB0_491

.LBB0_489:
	s_add_u32 s36, s30, 0x80
	s_addc_u32 s37, s31, 0
	s_waitcnt lgkmcnt(0)
	s_and_b64 s[2:3], s[34:35], exec
	s_cselect_b32 s37, s9, s37
	s_cselect_b32 s36, s8, s36
	s_cselect_b32 s35, s25, s69
	s_cselect_b32 s34, s24, s68
	s_barrier
	s_waitcnt lgkmcnt(0)
	v_mfma_f32_16x16x128_f8f6f4 v[190:193], v[18:25], v[58:65], v[190:193]
	v_mfma_f32_16x16x128_f8f6f4 v[186:189], v[26:33], v[58:65], v[186:189]
	v_mfma_f32_16x16x128_f8f6f4 v[174:177], v[18:25], v[50:57], v[174:177]
	v_mfma_f32_16x16x128_f8f6f4 v[170:173], v[26:33], v[50:57], v[170:173]
	v_mfma_f32_16x16x128_f8f6f4 v[158:161], v[18:25], v[42:49], v[158:161]
	v_mfma_f32_16x16x128_f8f6f4 v[154:157], v[26:33], v[42:49], v[154:157]
	v_mfma_f32_16x16x128_f8f6f4 v[142:145], v[18:25], v[34:41], v[142:145]
	v_mfma_f32_16x16x128_f8f6f4 v[138:141], v[26:33], v[34:41], v[138:141]
	v_mfma_f32_16x16x128_f8f6f4 v[182:185], v[2:9], v[58:65], v[182:185]
	v_mfma_f32_16x16x128_f8f6f4 v[178:181], v[10:17], v[58:65], v[178:181]
	v_mfma_f32_16x16x128_f8f6f4 v[166:169], v[2:9], v[50:57], v[166:169]
	v_mfma_f32_16x16x128_f8f6f4 v[162:165], v[10:17], v[50:57], v[162:165]
	v_mfma_f32_16x16x128_f8f6f4 v[150:153], v[2:9], v[42:49], v[150:153]
	v_mfma_f32_16x16x128_f8f6f4 v[146:149], v[10:17], v[42:49], v[146:149]
	v_mfma_f32_16x16x128_f8f6f4 v[134:137], v[2:9], v[34:41], v[134:137]
	v_mfma_f32_16x16x128_f8f6f4 v[130:133], v[10:17], v[34:41], v[130:133]
	s_barrier
	s_mov_b32 m0, s46
	v_lshl_add_u64 v[212:213], s[34:35], 0, v[194:195]
	s_add_u32 s2, s34, 0xa000
	ds_read_b128 v[58:61], v222 offset:16384
	ds_read_b128 v[62:65], v222 offset:16400
	ds_read_b128 v[50:53], v222 offset:18432
	ds_read_b128 v[54:57], v222 offset:18448
	ds_read_b128 v[42:45], v222 offset:20480
	ds_read_b128 v[46:49], v222 offset:20496
	ds_read_b128 v[34:37], v222 offset:22528
	ds_read_b128 v[38:41], v222 offset:22544
	global_load_lds_dwordx4 v[212:213], off
	v_lshl_add_u64 v[210:211], s[34:35], 0, v[196:197]
	s_mov_b32 m0, s47
	s_addc_u32 s3, s35, 0
	global_load_lds_dwordx4 v[210:211], off
	v_lshl_add_u64 v[224:225], s[2:3], 0, v[194:195]
	s_mov_b32 m0, s48
	s_andn2_b64 vcc, exec, s[38:39]
	global_load_lds_dwordx4 v[224:225], off
	v_lshl_add_u64 v[224:225], s[2:3], 0, v[196:197]
	s_mov_b32 m0, s49
	s_nop 0
	global_load_lds_dwordx4 v[224:225], off
	s_mov_b32 m0, s45
	s_nop 0
	global_load_lds_dwordx4 v198, s[36:37]
	s_mov_b32 m0, s50
	s_nop 0
	global_load_lds_dwordx4 v200, s[36:37]
	s_cbranch_vccnz .LBB0_482
	s_waitcnt vmcnt(8)
	s_branch .LBB0_482

.LBB0_570:
	s_mov_b32 s67, 0
	s_waitcnt lgkmcnt(0)
	v_mov_b32_e32 v201, v199
	v_lshl_add_u64 v[210:211], s[42:43], 0, v[198:199]
	v_lshl_add_u64 v[212:213], s[42:43], 0, v[200:201]
	s_barrier
	s_cmp_eq_u32 s66, -2
	s_cbranch_scc1 .Lnz_P4b_first
	s_waitcnt lgkmcnt(0)
	v_mfma_f32_16x16x128_f8f6f4 v[126:129], v[18:25], v[58:65], v[126:129]
	v_mfma_f32_16x16x128_f8f6f4 v[122:125], v[26:33], v[58:65], v[122:125]
	v_mfma_f32_16x16x128_f8f6f4 v[110:113], v[18:25], v[50:57], v[110:113]
	v_mfma_f32_16x16x128_f8f6f4 v[106:109], v[26:33], v[50:57], v[106:109]
	v_mfma_f32_16x16x128_f8f6f4 v[86:89], v[18:25], v[42:49], v[86:89]
	v_mfma_f32_16x16x128_f8f6f4 v[82:85], v[26:33], v[42:49], v[82:85]
	v_mfma_f32_16x16x128_f8f6f4 v[70:73], v[18:25], v[34:41], v[70:73]
	v_mfma_f32_16x16x128_f8f6f4 v[66:69], v[26:33], v[34:41], v[66:69]
	v_mfma_f32_16x16x128_f8f6f4 v[118:121], v[2:9], v[58:65], v[118:121]
	v_mfma_f32_16x16x128_f8f6f4 v[114:117], v[10:17], v[58:65], v[114:117]
	v_mfma_f32_16x16x128_f8f6f4 v[102:105], v[2:9], v[50:57], v[102:105]
	v_mfma_f32_16x16x128_f8f6f4 v[90:93], v[10:17], v[50:57], v[90:93]
	v_mfma_f32_16x16x128_f8f6f4 v[98:101], v[2:9], v[42:49], v[98:101]
	v_mfma_f32_16x16x128_f8f6f4 v[94:97], v[10:17], v[42:49], v[94:97]
	v_mfma_f32_16x16x128_f8f6f4 v[78:81], v[2:9], v[34:41], v[78:81]
	v_mfma_f32_16x16x128_f8f6f4 v[74:77], v[10:17], v[34:41], v[74:77]
.Lnz_P4b_back:
	s_barrier
	s_add_i32 s44, 0, 0x18000
	s_add_i32 s45, 0, 0x1c000
	v_add_u32_e32 v14, s44, v220
	v_add_u32_e32 v30, s45, v220
	ds_read_b128 v[2:5], v14
	ds_read_b128 v[6:9], v14 offset:16
	ds_read_b128 v[10:13], v14 offset:2048
	ds_read_b128 v[14:17], v14 offset:2064
	ds_read_b128 v[18:21], v30
	ds_read_b128 v[22:25], v30 offset:16
	ds_read_b128 v[26:29], v30 offset:2048
	ds_read_b128 v[30:33], v30 offset:2064
	s_mov_b32 m0, s55
	ds_read_b128 v[34:37], v225 offset:32768
	ds_read_b128 v[38:41], v225 offset:32784
	ds_read_b128 v[42:45], v225 offset:34816
	ds_read_b128 v[46:49], v225 offset:34832
	ds_read_b128 v[50:53], v225 offset:36864
	ds_read_b128 v[54:57], v225 offset:36880
	ds_read_b128 v[58:61], v225 offset:38912
	ds_read_b128 v[62:65], v225 offset:38928
	global_load_lds_dwordx4 v217, s[42:43]
	s_mov_b32 m0, s58
	s_nop 0
	global_load_lds_dwordx4 v218, s[42:43]
	s_waitcnt vmcnt(8)
	s_waitcnt lgkmcnt(0)
	s_barrier
	s_waitcnt lgkmcnt(0)
	v_mfma_f32_16x16x128_f8f6f4 v[190:193], v[2:9], v[34:41], v[190:193]
	v_mfma_f32_16x16x128_f8f6f4 v[186:189], v[10:17], v[34:41], v[186:189]
	v_mfma_f32_16x16x128_f8f6f4 v[174:177], v[2:9], v[42:49], v[174:177]
	v_mfma_f32_16x16x128_f8f6f4 v[170:173], v[10:17], v[42:49], v[170:173]
	v_mfma_f32_16x16x128_f8f6f4 v[158:161], v[2:9], v[50:57], v[158:161]
	v_mfma_f32_16x16x128_f8f6f4 v[154:157], v[10:17], v[50:57], v[154:157]
	v_mfma_f32_16x16x128_f8f6f4 v[142:145], v[2:9], v[58:65], v[142:145]
	v_mfma_f32_16x16x128_f8f6f4 v[138:141], v[10:17], v[58:65], v[138:141]
	v_mfma_f32_16x16x128_f8f6f4 v[182:185], v[18:25], v[34:41], v[182:185]
	v_mfma_f32_16x16x128_f8f6f4 v[178:181], v[26:33], v[34:41], v[178:181]
	v_mfma_f32_16x16x128_f8f6f4 v[166:169], v[18:25], v[42:49], v[166:169]
	v_mfma_f32_16x16x128_f8f6f4 v[162:165], v[26:33], v[42:49], v[162:165]
	v_mfma_f32_16x16x128_f8f6f4 v[150:153], v[18:25], v[50:57], v[150:153]
	v_mfma_f32_16x16x128_f8f6f4 v[146:149], v[26:33], v[50:57], v[146:149]
	v_mfma_f32_16x16x128_f8f6f4 v[134:137], v[18:25], v[58:65], v[134:137]
	v_mfma_f32_16x16x128_f8f6f4 v[130:133], v[26:33], v[58:65], v[130:133]
	s_barrier
	s_add_i32 s42, s44, s47
	v_lshl_add_u64 v[208:209], v[208:209], 0, s[20:21]
	s_mov_b32 m0, s42
	ds_read_b128 v[34:37], v225 offset:49152
	ds_read_b128 v[38:41], v225 offset:49168
	ds_read_b128 v[42:45], v225 offset:51200
	ds_read_b128 v[46:49], v225 offset:51216
	ds_read_b128 v[50:53], v225 offset:53248
	ds_read_b128 v[54:57], v225 offset:53264
	ds_read_b128 v[58:61], v225 offset:55296
	ds_read_b128 v[62:65], v225 offset:55312
	global_load_lds_dwordx4 v[208:209], off
	s_add_i32 m0, s42, 0x2000
	s_add_u32 s40, s40, 0x8080
	v_lshl_add_u64 v[206:207], v[206:207], 0, s[20:21]
	s_addc_u32 s41, s41, 0
	s_add_i32 s42, s45, s47
	global_load_lds_dwordx4 v[206:207], off
	v_lshl_add_u64 v[206:207], s[40:41], 0, v[194:195]
	s_mov_b32 m0, s42
	s_nop 0
	global_load_lds_dwordx4 v[206:207], off
	v_lshl_add_u64 v[206:207], s[40:41], 0, v[196:197]
	s_add_i32 m0, s42, 0x2000
	s_nop 0
	global_load_lds_dwordx4 v[206:207], off
	v_lshl_add_u64 v[206:207], v[210:211], 0, s[20:21]
	s_mov_b32 m0, s60
	s_nop 0
	global_load_lds_dwordx4 v[206:207], off
	v_lshl_add_u64 v[206:207], v[212:213], 0, s[20:21]
	s_mov_b32 m0, s61
	s_nop 0
	global_load_lds_dwordx4 v[206:207], off
	s_waitcnt vmcnt(8)
	s_waitcnt lgkmcnt(0)
	s_barrier
	s_waitcnt lgkmcnt(0)
	v_mfma_f32_16x16x128_f8f6f4 v[126:129], v[2:9], v[34:41], v[126:129]
	v_mfma_f32_16x16x128_f8f6f4 v[122:125], v[10:17], v[34:41], v[122:125]
	v_mfma_f32_16x16x128_f8f6f4 v[110:113], v[2:9], v[42:49], v[110:113]
	v_mfma_f32_16x16x128_f8f6f4 v[106:109], v[10:17], v[42:49], v[106:109]
	v_mfma_f32_16x16x128_f8f6f4 v[86:89], v[2:9], v[50:57], v[86:89]
	v_mfma_f32_16x16x128_f8f6f4 v[82:85], v[10:17], v[50:57], v[82:85]
	v_mfma_f32_16x16x128_f8f6f4 v[70:73], v[2:9], v[58:65], v[70:73]
	v_mfma_f32_16x16x128_f8f6f4 v[66:69], v[10:17], v[58:65], v[66:69]
	v_mfma_f32_16x16x128_f8f6f4 v[118:121], v[18:25], v[34:41], v[118:121]
	v_mfma_f32_16x16x128_f8f6f4 v[114:117], v[26:33], v[34:41], v[114:117]
	v_mfma_f32_16x16x128_f8f6f4 v[102:105], v[18:25], v[42:49], v[102:105]
	v_mfma_f32_16x16x128_f8f6f4 v[90:93], v[26:33], v[42:49], v[90:93]
	v_mfma_f32_16x16x128_f8f6f4 v[98:101], v[18:25], v[50:57], v[98:101]
	v_mfma_f32_16x16x128_f8f6f4 v[94:97], v[26:33], v[50:57], v[94:97]
	v_mfma_f32_16x16x128_f8f6f4 v[78:81], v[18:25], v[58:65], v[78:81]
	v_mfma_f32_16x16x128_f8f6f4 v[74:77], v[26:33], v[58:65], v[74:77]
	s_barrier
	s_add_i32 s66, s66, 2
	s_add_u32 s38, s38, 0x100
	s_addc_u32 s39, s39, 0
	s_add_u32 s64, s64, 0x100
	s_addc_u32 s65, s65, 0
	s_cmp_gt_u32 s66, 5
	s_cbranch_scc1 .LBB0_577

.LBB0_575:
	s_add_u32 s42, s38, 0x80
	s_addc_u32 s43, s39, 0
	s_waitcnt lgkmcnt(0)
	s_and_b64 s[40:41], s[40:41], exec
	s_cselect_b32 s43, s11, s43
	s_cselect_b32 s42, s10, s42
	s_cselect_b32 s41, s2, s65
	s_cselect_b32 s40, s9, s64
	s_barrier
	s_cmp_eq_u32 s66, -2
	s_cbranch_scc1 .Lnz_P4a_first
	s_waitcnt lgkmcnt(0)
	v_mfma_f32_16x16x128_f8f6f4 v[190:193], v[18:25], v[58:65], v[190:193]
	v_mfma_f32_16x16x128_f8f6f4 v[186:189], v[26:33], v[58:65], v[186:189]
	v_mfma_f32_16x16x128_f8f6f4 v[174:177], v[18:25], v[50:57], v[174:177]
	v_mfma_f32_16x16x128_f8f6f4 v[170:173], v[26:33], v[50:57], v[170:173]
	v_mfma_f32_16x16x128_f8f6f4 v[158:161], v[18:25], v[42:49], v[158:161]
	v_mfma_f32_16x16x128_f8f6f4 v[154:157], v[26:33], v[42:49], v[154:157]
	v_mfma_f32_16x16x128_f8f6f4 v[142:145], v[18:25], v[34:41], v[142:145]
	v_mfma_f32_16x16x128_f8f6f4 v[138:141], v[26:33], v[34:41], v[138:141]
	v_mfma_f32_16x16x128_f8f6f4 v[182:185], v[2:9], v[58:65], v[182:185]
	v_mfma_f32_16x16x128_f8f6f4 v[178:181], v[10:17], v[58:65], v[178:181]
	v_mfma_f32_16x16x128_f8f6f4 v[166:169], v[2:9], v[50:57], v[166:169]
	v_mfma_f32_16x16x128_f8f6f4 v[162:165], v[10:17], v[50:57], v[162:165]
	v_mfma_f32_16x16x128_f8f6f4 v[150:153], v[2:9], v[42:49], v[150:153]
	v_mfma_f32_16x16x128_f8f6f4 v[146:149], v[10:17], v[42:49], v[146:149]
	v_mfma_f32_16x16x128_f8f6f4 v[134:137], v[2:9], v[34:41], v[134:137]
	v_mfma_f32_16x16x128_f8f6f4 v[130:133], v[10:17], v[34:41], v[130:133]

.LBB0_985:
	s_mov_b32 s88, 0
	s_waitcnt lgkmcnt(0)
	v_mov_b32_e32 v201, v199
	v_lshl_add_u64 v[210:211], s[46:47], 0, v[198:199]
	v_lshl_add_u64 v[212:213], s[46:47], 0, v[200:201]
	s_barrier
	s_cmp_eq_u32 s87, -2
	s_cbranch_scc1 .Lnz_P7b_first
	s_waitcnt lgkmcnt(0)
	v_mfma_f32_16x16x128_f8f6f4 v[126:129], v[18:25], v[58:65], v[126:129]
	v_mfma_f32_16x16x128_f8f6f4 v[122:125], v[26:33], v[58:65], v[122:125]
	v_mfma_f32_16x16x128_f8f6f4 v[110:113], v[18:25], v[50:57], v[110:113]
	v_mfma_f32_16x16x128_f8f6f4 v[106:109], v[26:33], v[50:57], v[106:109]
	v_mfma_f32_16x16x128_f8f6f4 v[86:89], v[18:25], v[42:49], v[86:89]
	v_mfma_f32_16x16x128_f8f6f4 v[82:85], v[26:33], v[42:49], v[82:85]
	v_mfma_f32_16x16x128_f8f6f4 v[70:73], v[18:25], v[34:41], v[70:73]
	v_mfma_f32_16x16x128_f8f6f4 v[66:69], v[26:33], v[34:41], v[66:69]
	v_mfma_f32_16x16x128_f8f6f4 v[118:121], v[2:9], v[58:65], v[118:121]
	v_mfma_f32_16x16x128_f8f6f4 v[114:117], v[10:17], v[58:65], v[114:117]
	v_mfma_f32_16x16x128_f8f6f4 v[102:105], v[2:9], v[50:57], v[102:105]
	v_mfma_f32_16x16x128_f8f6f4 v[90:93], v[10:17], v[50:57], v[90:93]
	v_mfma_f32_16x16x128_f8f6f4 v[94:97], v[2:9], v[42:49], v[94:97]
	v_mfma_f32_16x16x128_f8f6f4 v[98:101], v[10:17], v[42:49], v[98:101]
	v_mfma_f32_16x16x128_f8f6f4 v[74:77], v[2:9], v[34:41], v[74:77]
	v_mfma_f32_16x16x128_f8f6f4 v[78:81], v[10:17], v[34:41], v[78:81]
.Lnz_P7b_back:
	s_barrier
	s_add_i32 s48, 0, 0x18000
	s_add_i32 s49, 0, 0x1c000
	v_add_u32_e32 v14, s48, v217
	v_add_u32_e32 v30, s49, v217
	ds_read_b128 v[2:5], v14
	ds_read_b128 v[6:9], v14 offset:16
	ds_read_b128 v[10:13], v14 offset:2048
	ds_read_b128 v[14:17], v14 offset:2064
	ds_read_b128 v[18:21], v30
	ds_read_b128 v[22:25], v30 offset:16
	ds_read_b128 v[26:29], v30 offset:2048
	ds_read_b128 v[30:33], v30 offset:2064
	s_mov_b32 m0, s65
	ds_read_b128 v[34:37], v222 offset:32768
	ds_read_b128 v[38:41], v222 offset:32784
	ds_read_b128 v[42:45], v222 offset:34816
	ds_read_b128 v[46:49], v222 offset:34832
	ds_read_b128 v[50:53], v222 offset:36864
	ds_read_b128 v[54:57], v222 offset:36880
	ds_read_b128 v[58:61], v222 offset:38912
	ds_read_b128 v[62:65], v222 offset:38928
	global_load_lds_dwordx4 v215, s[46:47]
	s_mov_b32 m0, s66
	s_nop 0
	global_load_lds_dwordx4 v216, s[46:47]
	s_waitcnt vmcnt(8)
	s_waitcnt lgkmcnt(0)
	s_barrier
	s_waitcnt lgkmcnt(0)
	v_mfma_f32_16x16x128_f8f6f4 v[190:193], v[2:9], v[34:41], v[190:193]
	v_mfma_f32_16x16x128_f8f6f4 v[186:189], v[10:17], v[34:41], v[186:189]
	v_mfma_f32_16x16x128_f8f6f4 v[174:177], v[2:9], v[42:49], v[174:177]
	v_mfma_f32_16x16x128_f8f6f4 v[170:173], v[10:17], v[42:49], v[170:173]
	v_mfma_f32_16x16x128_f8f6f4 v[158:161], v[2:9], v[50:57], v[158:161]
	v_mfma_f32_16x16x128_f8f6f4 v[154:157], v[10:17], v[50:57], v[154:157]
	v_mfma_f32_16x16x128_f8f6f4 v[142:145], v[2:9], v[58:65], v[142:145]
	v_mfma_f32_16x16x128_f8f6f4 v[138:141], v[10:17], v[58:65], v[138:141]
	v_mfma_f32_16x16x128_f8f6f4 v[182:185], v[18:25], v[34:41], v[182:185]
	v_mfma_f32_16x16x128_f8f6f4 v[178:181], v[26:33], v[34:41], v[178:181]
	v_mfma_f32_16x16x128_f8f6f4 v[166:169], v[18:25], v[42:49], v[166:169]
	v_mfma_f32_16x16x128_f8f6f4 v[162:165], v[26:33], v[42:49], v[162:165]
	v_mfma_f32_16x16x128_f8f6f4 v[150:153], v[18:25], v[50:57], v[150:153]
	v_mfma_f32_16x16x128_f8f6f4 v[146:149], v[26:33], v[50:57], v[146:149]
	v_mfma_f32_16x16x128_f8f6f4 v[134:137], v[18:25], v[58:65], v[134:137]
	v_mfma_f32_16x16x128_f8f6f4 v[130:133], v[26:33], v[58:65], v[130:133]
	s_barrier
	s_add_i32 s46, s48, s52
	v_lshl_add_u64 v[208:209], v[208:209], 0, s[20:21]
	s_mov_b32 m0, s46
	ds_read_b128 v[34:37], v222 offset:49152
	ds_read_b128 v[38:41], v222 offset:49168
	ds_read_b128 v[42:45], v222 offset:51200
	ds_read_b128 v[46:49], v222 offset:51216
	ds_read_b128 v[50:53], v222 offset:53248
	ds_read_b128 v[54:57], v222 offset:53264
	ds_read_b128 v[58:61], v222 offset:55296
	ds_read_b128 v[62:65], v222 offset:55312
	global_load_lds_dwordx4 v[208:209], off
	s_add_i32 m0, s46, 0x2000
	s_add_u32 s44, s44, 0x20080
	v_lshl_add_u64 v[206:207], v[206:207], 0, s[20:21]
	s_addc_u32 s45, s45, 0
	s_add_i32 s46, s49, s52
	global_load_lds_dwordx4 v[206:207], off
	v_lshl_add_u64 v[206:207], s[44:45], 0, v[194:195]
	s_mov_b32 m0, s46
	s_nop 0
	global_load_lds_dwordx4 v[206:207], off
	v_lshl_add_u64 v[206:207], s[44:45], 0, v[196:197]
	s_add_i32 m0, s46, 0x2000
	s_nop 0
	global_load_lds_dwordx4 v[206:207], off
	v_lshl_add_u64 v[206:207], v[210:211], 0, s[20:21]
	s_mov_b32 m0, s68
	s_nop 0
	global_load_lds_dwordx4 v[206:207], off
	v_lshl_add_u64 v[206:207], v[212:213], 0, s[20:21]
	s_mov_b32 m0, s69
	s_nop 0
	global_load_lds_dwordx4 v[206:207], off
	s_waitcnt vmcnt(8)
	s_waitcnt lgkmcnt(0)
	s_barrier
	s_waitcnt lgkmcnt(0)
	v_mfma_f32_16x16x128_f8f6f4 v[126:129], v[2:9], v[34:41], v[126:129]
	v_mfma_f32_16x16x128_f8f6f4 v[122:125], v[10:17], v[34:41], v[122:125]
	v_mfma_f32_16x16x128_f8f6f4 v[110:113], v[2:9], v[42:49], v[110:113]
	v_mfma_f32_16x16x128_f8f6f4 v[106:109], v[10:17], v[42:49], v[106:109]
	v_mfma_f32_16x16x128_f8f6f4 v[86:89], v[2:9], v[50:57], v[86:89]
	v_mfma_f32_16x16x128_f8f6f4 v[82:85], v[10:17], v[50:57], v[82:85]
	v_mfma_f32_16x16x128_f8f6f4 v[70:73], v[2:9], v[58:65], v[70:73]
	v_mfma_f32_16x16x128_f8f6f4 v[66:69], v[10:17], v[58:65], v[66:69]
	v_mfma_f32_16x16x128_f8f6f4 v[118:121], v[18:25], v[34:41], v[118:121]
	v_mfma_f32_16x16x128_f8f6f4 v[114:117], v[26:33], v[34:41], v[114:117]
	v_mfma_f32_16x16x128_f8f6f4 v[102:105], v[18:25], v[42:49], v[102:105]
	v_mfma_f32_16x16x128_f8f6f4 v[90:93], v[26:33], v[42:49], v[90:93]
	v_mfma_f32_16x16x128_f8f6f4 v[94:97], v[18:25], v[50:57], v[94:97]
	v_mfma_f32_16x16x128_f8f6f4 v[98:101], v[26:33], v[50:57], v[98:101]
	v_mfma_f32_16x16x128_f8f6f4 v[74:77], v[18:25], v[58:65], v[74:77]
	v_mfma_f32_16x16x128_f8f6f4 v[78:81], v[26:33], v[58:65], v[78:81]
	s_barrier
	s_add_i32 s87, s87, 2
	s_add_u32 s38, s38, 0x100
	s_addc_u32 s39, s39, 0
	s_add_u32 s85, s85, 0x100
	s_addc_u32 s86, s86, 0
	s_cmp_gt_u32 s87, 5
	s_cbranch_scc1 .LBB0_992

.LBB0_990:
	s_add_u32 s46, s38, 0x80
	s_addc_u32 s47, s39, 0
	s_waitcnt lgkmcnt(0)
	s_and_b64 s[44:45], s[44:45], exec
	s_cselect_b32 s47, s15, s47
	s_cselect_b32 s46, s14, s46
	s_cselect_b32 s45, s2, s86
	s_cselect_b32 s44, s11, s85
	s_barrier
	s_cmp_eq_u32 s87, -2
	s_cbranch_scc1 .Lnz_P7a_first
	s_waitcnt lgkmcnt(0)
	v_mfma_f32_16x16x128_f8f6f4 v[190:193], v[18:25], v[58:65], v[190:193]
	v_mfma_f32_16x16x128_f8f6f4 v[186:189], v[26:33], v[58:65], v[186:189]
	v_mfma_f32_16x16x128_f8f6f4 v[174:177], v[18:25], v[50:57], v[174:177]
	v_mfma_f32_16x16x128_f8f6f4 v[170:173], v[26:33], v[50:57], v[170:173]
	v_mfma_f32_16x16x128_f8f6f4 v[158:161], v[18:25], v[42:49], v[158:161]
	v_mfma_f32_16x16x128_f8f6f4 v[154:157], v[26:33], v[42:49], v[154:157]
	v_mfma_f32_16x16x128_f8f6f4 v[142:145], v[18:25], v[34:41], v[142:145]
	v_mfma_f32_16x16x128_f8f6f4 v[138:141], v[26:33], v[34:41], v[138:141]
	v_mfma_f32_16x16x128_f8f6f4 v[182:185], v[2:9], v[58:65], v[182:185]
	v_mfma_f32_16x16x128_f8f6f4 v[178:181], v[10:17], v[58:65], v[178:181]
	v_mfma_f32_16x16x128_f8f6f4 v[166:169], v[2:9], v[50:57], v[166:169]
	v_mfma_f32_16x16x128_f8f6f4 v[162:165], v[10:17], v[50:57], v[162:165]
	v_mfma_f32_16x16x128_f8f6f4 v[150:153], v[2:9], v[42:49], v[150:153]
	v_mfma_f32_16x16x128_f8f6f4 v[146:149], v[10:17], v[42:49], v[146:149]
	v_mfma_f32_16x16x128_f8f6f4 v[134:137], v[2:9], v[34:41], v[134:137]
	v_mfma_f32_16x16x128_f8f6f4 v[130:133], v[10:17], v[34:41], v[130:133]

.LBB0_1081:
	s_mov_b32 s35, 0
	s_waitcnt lgkmcnt(0)
	v_mov_b32_e32 v201, v199
	v_lshl_add_u64 v[208:209], s[52:53], 0, v[198:199]
	v_lshl_add_u64 v[210:211], s[52:53], 0, v[200:201]
	s_barrier
	s_cmp_eq_u32 s34, -2
	s_cbranch_scc1 .Lnz_P8b_first
	s_waitcnt lgkmcnt(0)
	v_mfma_f32_16x16x128_f8f6f4 v[126:129], v[18:25], v[58:65], v[126:129]
	v_mfma_f32_16x16x128_f8f6f4 v[122:125], v[26:33], v[58:65], v[122:125]
	v_mfma_f32_16x16x128_f8f6f4 v[106:109], v[18:25], v[50:57], v[106:109]
	v_mfma_f32_16x16x128_f8f6f4 v[98:101], v[26:33], v[50:57], v[98:101]
	v_mfma_f32_16x16x128_f8f6f4 v[78:81], v[18:25], v[42:49], v[78:81]
	v_mfma_f32_16x16x128_f8f6f4 v[74:77], v[26:33], v[42:49], v[74:77]
	v_mfma_f32_16x16x128_f8f6f4 v[70:73], v[18:25], v[34:41], v[70:73]
	v_mfma_f32_16x16x128_f8f6f4 v[66:69], v[26:33], v[34:41], v[66:69]
	v_mfma_f32_16x16x128_f8f6f4 v[118:121], v[2:9], v[58:65], v[118:121]
	v_mfma_f32_16x16x128_f8f6f4 v[114:117], v[10:17], v[58:65], v[114:117]
	v_mfma_f32_16x16x128_f8f6f4 v[90:93], v[2:9], v[50:57], v[90:93]
	v_mfma_f32_16x16x128_f8f6f4 v[82:85], v[10:17], v[50:57], v[82:85]
	v_mfma_f32_16x16x128_f8f6f4 v[102:105], v[2:9], v[42:49], v[102:105]
	v_mfma_f32_16x16x128_f8f6f4 v[110:113], v[10:17], v[42:49], v[110:113]
	v_mfma_f32_16x16x128_f8f6f4 v[86:89], v[2:9], v[34:41], v[86:89]
	v_mfma_f32_16x16x128_f8f6f4 v[94:97], v[10:17], v[34:41], v[94:97]
.Lnz_P8b_back:
	s_barrier
	s_add_i32 s54, 0, 0x18000
	s_add_i32 s55, 0, 0x1c000
	v_add_u32_e32 v14, s54, v216
	v_add_u32_e32 v30, s55, v216
	ds_read_b128 v[2:5], v14
	ds_read_b128 v[6:9], v14 offset:16
	ds_read_b128 v[10:13], v14 offset:2048
	ds_read_b128 v[14:17], v14 offset:2064
	ds_read_b128 v[18:21], v30
	ds_read_b128 v[22:25], v30 offset:16
	ds_read_b128 v[26:29], v30 offset:2048
	ds_read_b128 v[30:33], v30 offset:2064
	s_mov_b32 m0, s20
	ds_read_b128 v[34:37], v220 offset:32768
	ds_read_b128 v[38:41], v220 offset:32784
	ds_read_b128 v[42:45], v220 offset:34816
	ds_read_b128 v[46:49], v220 offset:34832
	ds_read_b128 v[50:53], v220 offset:36864
	ds_read_b128 v[54:57], v220 offset:36880
	ds_read_b128 v[58:61], v220 offset:38912
	ds_read_b128 v[62:65], v220 offset:38928
	global_load_lds_dwordx4 v213, s[52:53]
	s_mov_b32 m0, s21
	s_nop 0
	global_load_lds_dwordx4 v214, s[52:53]
	s_waitcnt vmcnt(8)
	s_waitcnt lgkmcnt(0)
	s_barrier
	s_waitcnt lgkmcnt(0)
	v_mfma_f32_16x16x128_f8f6f4 v[190:193], v[2:9], v[34:41], v[190:193]
	v_mfma_f32_16x16x128_f8f6f4 v[186:189], v[10:17], v[34:41], v[186:189]
	v_mfma_f32_16x16x128_f8f6f4 v[182:185], v[2:9], v[42:49], v[182:185]
	v_mfma_f32_16x16x128_f8f6f4 v[178:181], v[10:17], v[42:49], v[178:181]
	v_mfma_f32_16x16x128_f8f6f4 v[158:161], v[2:9], v[50:57], v[158:161]
	v_mfma_f32_16x16x128_f8f6f4 v[154:157], v[10:17], v[50:57], v[154:157]
	v_mfma_f32_16x16x128_f8f6f4 v[142:145], v[2:9], v[58:65], v[142:145]
	v_mfma_f32_16x16x128_f8f6f4 v[138:141], v[10:17], v[58:65], v[138:141]
	v_mfma_f32_16x16x128_f8f6f4 v[174:177], v[18:25], v[34:41], v[174:177]
	v_mfma_f32_16x16x128_f8f6f4 v[170:173], v[26:33], v[34:41], v[170:173]
	v_mfma_f32_16x16x128_f8f6f4 v[166:169], v[18:25], v[42:49], v[166:169]
	v_mfma_f32_16x16x128_f8f6f4 v[162:165], v[26:33], v[42:49], v[162:165]
	v_mfma_f32_16x16x128_f8f6f4 v[150:153], v[18:25], v[50:57], v[150:153]
	v_mfma_f32_16x16x128_f8f6f4 v[146:149], v[26:33], v[50:57], v[146:149]
	v_mfma_f32_16x16x128_f8f6f4 v[134:137], v[18:25], v[58:65], v[134:137]
	v_mfma_f32_16x16x128_f8f6f4 v[130:133], v[26:33], v[58:65], v[130:133]
	s_barrier
	s_add_i32 s52, s54, s69
	v_lshl_add_u64 v[206:207], v[206:207], 0, s[38:39]
	s_mov_b32 m0, s52
	ds_read_b128 v[34:37], v220 offset:49152
	ds_read_b128 v[38:41], v220 offset:49168
	ds_read_b128 v[42:45], v220 offset:51200
	ds_read_b128 v[46:49], v220 offset:51216
	ds_read_b128 v[50:53], v220 offset:53248
	ds_read_b128 v[54:57], v220 offset:53264
	ds_read_b128 v[58:61], v220 offset:55296
	ds_read_b128 v[62:65], v220 offset:55312
	global_load_lds_dwordx4 v[206:207], off
	s_add_i32 m0, s52, 0x2000
	s_add_u32 s50, s50, 0x8080
	v_lshl_add_u64 v[204:205], v[204:205], 0, s[38:39]
	s_addc_u32 s51, s51, 0
	s_add_i32 s52, s55, s69
	global_load_lds_dwordx4 v[204:205], off
	v_lshl_add_u64 v[204:205], s[50:51], 0, v[194:195]
	s_mov_b32 m0, s52
	s_nop 0
	global_load_lds_dwordx4 v[204:205], off
	v_lshl_add_u64 v[204:205], s[50:51], 0, v[196:197]
	s_add_i32 m0, s52, 0x2000
	s_nop 0
	global_load_lds_dwordx4 v[204:205], off
	v_lshl_add_u64 v[204:205], v[208:209], 0, s[38:39]
	s_mov_b32 m0, s22
	s_nop 0
	global_load_lds_dwordx4 v[204:205], off
	v_lshl_add_u64 v[204:205], v[210:211], 0, s[38:39]
	s_mov_b32 m0, s23
	s_nop 0
	global_load_lds_dwordx4 v[204:205], off
	s_waitcnt vmcnt(8)
	s_waitcnt lgkmcnt(0)
	s_barrier
	s_waitcnt lgkmcnt(0)
	v_mfma_f32_16x16x128_f8f6f4 v[126:129], v[2:9], v[34:41], v[126:129]
	v_mfma_f32_16x16x128_f8f6f4 v[122:125], v[10:17], v[34:41], v[122:125]
	v_mfma_f32_16x16x128_f8f6f4 v[106:109], v[2:9], v[42:49], v[106:109]
	v_mfma_f32_16x16x128_f8f6f4 v[98:101], v[10:17], v[42:49], v[98:101]
	v_mfma_f32_16x16x128_f8f6f4 v[78:81], v[2:9], v[50:57], v[78:81]
	v_mfma_f32_16x16x128_f8f6f4 v[74:77], v[10:17], v[50:57], v[74:77]
	v_mfma_f32_16x16x128_f8f6f4 v[70:73], v[2:9], v[58:65], v[70:73]
	v_mfma_f32_16x16x128_f8f6f4 v[66:69], v[10:17], v[58:65], v[66:69]
	v_mfma_f32_16x16x128_f8f6f4 v[118:121], v[18:25], v[34:41], v[118:121]
	v_mfma_f32_16x16x128_f8f6f4 v[114:117], v[26:33], v[34:41], v[114:117]
	v_mfma_f32_16x16x128_f8f6f4 v[90:93], v[18:25], v[42:49], v[90:93]
	v_mfma_f32_16x16x128_f8f6f4 v[82:85], v[26:33], v[42:49], v[82:85]
	v_mfma_f32_16x16x128_f8f6f4 v[102:105], v[18:25], v[50:57], v[102:105]
	v_mfma_f32_16x16x128_f8f6f4 v[110:113], v[26:33], v[50:57], v[110:113]
	v_mfma_f32_16x16x128_f8f6f4 v[86:89], v[18:25], v[58:65], v[86:89]
	v_mfma_f32_16x16x128_f8f6f4 v[94:97], v[26:33], v[58:65], v[94:97]
	s_barrier
	s_add_i32 s34, s34, 2
	s_add_u32 s78, s78, 0x100
	s_addc_u32 s79, s79, 0
	s_add_u32 s30, s30, 0x100
	s_addc_u32 s31, s31, 0
	s_cmp_gt_u32 s34, 5
	s_cbranch_scc1 .LBB0_1088

.LBB0_1086:
	s_add_u32 s35, s78, 0x80
	s_addc_u32 s52, s79, 0
	s_waitcnt lgkmcnt(0)
	s_and_b64 s[50:51], s[50:51], exec
	s_cselect_b32 s53, s59, s52
	s_cselect_b32 s52, s58, s35
	s_cselect_b32 s51, s57, s31
	s_cselect_b32 s50, s82, s30
	s_barrier
	s_cmp_eq_u32 s34, -2
	s_cbranch_scc1 .Lnz_P8a_first
	s_waitcnt lgkmcnt(0)
	v_mfma_f32_16x16x128_f8f6f4 v[190:193], v[18:25], v[58:65], v[190:193]
	v_mfma_f32_16x16x128_f8f6f4 v[186:189], v[26:33], v[58:65], v[186:189]
	v_mfma_f32_16x16x128_f8f6f4 v[182:185], v[18:25], v[50:57], v[182:185]
	v_mfma_f32_16x16x128_f8f6f4 v[178:181], v[26:33], v[50:57], v[178:181]
	v_mfma_f32_16x16x128_f8f6f4 v[158:161], v[18:25], v[42:49], v[158:161]
	v_mfma_f32_16x16x128_f8f6f4 v[154:157], v[26:33], v[42:49], v[154:157]
	v_mfma_f32_16x16x128_f8f6f4 v[142:145], v[18:25], v[34:41], v[142:145]
	v_mfma_f32_16x16x128_f8f6f4 v[138:141], v[26:33], v[34:41], v[138:141]
	v_mfma_f32_16x16x128_f8f6f4 v[174:177], v[2:9], v[58:65], v[174:177]
	v_mfma_f32_16x16x128_f8f6f4 v[170:173], v[10:17], v[58:65], v[170:173]
	v_mfma_f32_16x16x128_f8f6f4 v[166:169], v[2:9], v[50:57], v[166:169]
	v_mfma_f32_16x16x128_f8f6f4 v[162:165], v[10:17], v[50:57], v[162:165]
	v_mfma_f32_16x16x128_f8f6f4 v[150:153], v[2:9], v[42:49], v[150:153]
	v_mfma_f32_16x16x128_f8f6f4 v[146:149], v[10:17], v[42:49], v[146:149]
	v_mfma_f32_16x16x128_f8f6f4 v[134:137], v[2:9], v[34:41], v[134:137]
	v_mfma_f32_16x16x128_f8f6f4 v[130:133], v[10:17], v[34:41], v[130:133]

.Lnz_P1a_first:
	s_waitcnt lgkmcnt(0)
	v_mfma_f32_16x16x128_f8f6f4 v[190:193], v[18:25], v[58:65], 0
	v_mfma_f32_16x16x128_f8f6f4 v[186:189], v[26:33], v[58:65], 0
	v_mfma_f32_16x16x128_f8f6f4 v[174:177], v[18:25], v[50:57], 0
	v_mfma_f32_16x16x128_f8f6f4 v[170:173], v[26:33], v[50:57], 0
	v_mfma_f32_16x16x128_f8f6f4 v[158:161], v[18:25], v[42:49], 0
	v_mfma_f32_16x16x128_f8f6f4 v[154:157], v[26:33], v[42:49], 0
	v_mfma_f32_16x16x128_f8f6f4 v[142:145], v[18:25], v[34:41], 0
	v_mfma_f32_16x16x128_f8f6f4 v[138:141], v[26:33], v[34:41], 0
	v_mfma_f32_16x16x128_f8f6f4 v[182:185], v[2:9], v[58:65], 0
	v_mfma_f32_16x16x128_f8f6f4 v[178:181], v[10:17], v[58:65], 0
	v_mfma_f32_16x16x128_f8f6f4 v[166:169], v[2:9], v[50:57], 0
	v_mfma_f32_16x16x128_f8f6f4 v[162:165], v[10:17], v[50:57], 0
	v_mfma_f32_16x16x128_f8f6f4 v[150:153], v[2:9], v[42:49], 0
	v_mfma_f32_16x16x128_f8f6f4 v[146:149], v[10:17], v[42:49], 0
	v_mfma_f32_16x16x128_f8f6f4 v[134:137], v[2:9], v[34:41], 0
	v_mfma_f32_16x16x128_f8f6f4 v[130:133], v[10:17], v[34:41], 0
	s_branch .Lnz_P1a_back
.Lnz_P1b_first:
	s_waitcnt lgkmcnt(0)
	v_mfma_f32_16x16x128_f8f6f4 v[126:129], v[18:25], v[58:65], 0
	v_mfma_f32_16x16x128_f8f6f4 v[122:125], v[26:33], v[58:65], 0
	v_mfma_f32_16x16x128_f8f6f4 v[110:113], v[18:25], v[50:57], 0
	v_mfma_f32_16x16x128_f8f6f4 v[106:109], v[26:33], v[50:57], 0
	v_mfma_f32_16x16x128_f8f6f4 v[78:81], v[18:25], v[42:49], 0
	v_mfma_f32_16x16x128_f8f6f4 v[74:77], v[26:33], v[42:49], 0
	v_mfma_f32_16x16x128_f8f6f4 v[70:73], v[18:25], v[34:41], 0
	v_mfma_f32_16x16x128_f8f6f4 v[66:69], v[26:33], v[34:41], 0
	v_mfma_f32_16x16x128_f8f6f4 v[118:121], v[2:9], v[58:65], 0
	v_mfma_f32_16x16x128_f8f6f4 v[114:117], v[10:17], v[58:65], 0
	v_mfma_f32_16x16x128_f8f6f4 v[94:97], v[2:9], v[50:57], 0
	v_mfma_f32_16x16x128_f8f6f4 v[90:93], v[10:17], v[50:57], 0
	v_mfma_f32_16x16x128_f8f6f4 v[98:101], v[2:9], v[42:49], 0
	v_mfma_f32_16x16x128_f8f6f4 v[102:105], v[10:17], v[42:49], 0
	v_mfma_f32_16x16x128_f8f6f4 v[82:85], v[2:9], v[34:41], 0
	v_mfma_f32_16x16x128_f8f6f4 v[86:89], v[10:17], v[34:41], 0
	s_branch .Lnz_P1b_back

.Lnz_P4b_first:
	s_waitcnt lgkmcnt(0)
	v_mfma_f32_16x16x128_f8f6f4 v[126:129], v[18:25], v[58:65], 0
	v_mfma_f32_16x16x128_f8f6f4 v[122:125], v[26:33], v[58:65], 0
	v_mfma_f32_16x16x128_f8f6f4 v[110:113], v[18:25], v[50:57], 0
	v_mfma_f32_16x16x128_f8f6f4 v[106:109], v[26:33], v[50:57], 0
	v_mfma_f32_16x16x128_f8f6f4 v[86:89], v[18:25], v[42:49], 0
	v_mfma_f32_16x16x128_f8f6f4 v[82:85], v[26:33], v[42:49], 0
	v_mfma_f32_16x16x128_f8f6f4 v[70:73], v[18:25], v[34:41], 0
	v_mfma_f32_16x16x128_f8f6f4 v[66:69], v[26:33], v[34:41], 0
	v_mfma_f32_16x16x128_f8f6f4 v[118:121], v[2:9], v[58:65], 0
	v_mfma_f32_16x16x128_f8f6f4 v[114:117], v[10:17], v[58:65], 0
	v_mfma_f32_16x16x128_f8f6f4 v[102:105], v[2:9], v[50:57], 0
	v_mfma_f32_16x16x128_f8f6f4 v[90:93], v[10:17], v[50:57], 0
	v_mfma_f32_16x16x128_f8f6f4 v[98:101], v[2:9], v[42:49], 0
	v_mfma_f32_16x16x128_f8f6f4 v[94:97], v[10:17], v[42:49], 0
	v_mfma_f32_16x16x128_f8f6f4 v[78:81], v[2:9], v[34:41], 0
	v_mfma_f32_16x16x128_f8f6f4 v[74:77], v[10:17], v[34:41], 0
	s_branch .Lnz_P4b_back

.Lnz_P7b_first:
	s_waitcnt lgkmcnt(0)
	v_mfma_f32_16x16x128_f8f6f4 v[126:129], v[18:25], v[58:65], 0
	v_mfma_f32_16x16x128_f8f6f4 v[122:125], v[26:33], v[58:65], 0
	v_mfma_f32_16x16x128_f8f6f4 v[110:113], v[18:25], v[50:57], 0
	v_mfma_f32_16x16x128_f8f6f4 v[106:109], v[26:33], v[50:57], 0
	v_mfma_f32_16x16x128_f8f6f4 v[86:89], v[18:25], v[42:49], 0
	v_mfma_f32_16x16x128_f8f6f4 v[82:85], v[26:33], v[42:49], 0
	v_mfma_f32_16x16x128_f8f6f4 v[70:73], v[18:25], v[34:41], 0
	v_mfma_f32_16x16x128_f8f6f4 v[66:69], v[26:33], v[34:41], 0
	v_mfma_f32_16x16x128_f8f6f4 v[118:121], v[2:9], v[58:65], 0
	v_mfma_f32_16x16x128_f8f6f4 v[114:117], v[10:17], v[58:65], 0
	v_mfma_f32_16x16x128_f8f6f4 v[102:105], v[2:9], v[50:57], 0
	v_mfma_f32_16x16x128_f8f6f4 v[90:93], v[10:17], v[50:57], 0
	v_mfma_f32_16x16x128_f8f6f4 v[94:97], v[2:9], v[42:49], 0
	v_mfma_f32_16x16x128_f8f6f4 v[98:101], v[10:17], v[42:49], 0
	v_mfma_f32_16x16x128_f8f6f4 v[74:77], v[2:9], v[34:41], 0
	v_mfma_f32_16x16x128_f8f6f4 v[78:81], v[10:17], v[34:41], 0
	s_branch .Lnz_P7b_back
.Lnz_P8a_first:
	s_waitcnt lgkmcnt(0)
	v_mfma_f32_16x16x128_f8f6f4 v[190:193], v[18:25], v[58:65], 0
	v_mfma_f32_16x16x128_f8f6f4 v[186:189], v[26:33], v[58:65], 0
	v_mfma_f32_16x16x128_f8f6f4 v[182:185], v[18:25], v[50:57], 0
	v_mfma_f32_16x16x128_f8f6f4 v[178:181], v[26:33], v[50:57], 0
	v_mfma_f32_16x16x128_f8f6f4 v[158:161], v[18:25], v[42:49], 0
	v_mfma_f32_16x16x128_f8f6f4 v[154:157], v[26:33], v[42:49], 0
	v_mfma_f32_16x16x128_f8f6f4 v[142:145], v[18:25], v[34:41], 0
	v_mfma_f32_16x16x128_f8f6f4 v[138:141], v[26:33], v[34:41], 0
	v_mfma_f32_16x16x128_f8f6f4 v[174:177], v[2:9], v[58:65], 0
	v_mfma_f32_16x16x128_f8f6f4 v[170:173], v[10:17], v[58:65], 0
	v_mfma_f32_16x16x128_f8f6f4 v[166:169], v[2:9], v[50:57], 0
	v_mfma_f32_16x16x128_f8f6f4 v[162:165], v[10:17], v[50:57], 0
	v_mfma_f32_16x16x128_f8f6f4 v[150:153], v[2:9], v[42:49], 0
	v_mfma_f32_16x16x128_f8f6f4 v[146:149], v[10:17], v[42:49], 0
	v_mfma_f32_16x16x128_f8f6f4 v[134:137], v[2:9], v[34:41], 0
	v_mfma_f32_16x16x128_f8f6f4 v[130:133], v[10:17], v[34:41], 0
	s_branch .Lnz_P8a_back
.Lnz_P8b_first:
	s_waitcnt lgkmcnt(0)
	v_mfma_f32_16x16x128_f8f6f4 v[126:129], v[18:25], v[58:65], 0
	v_mfma_f32_16x16x128_f8f6f4 v[122:125], v[26:33], v[58:65], 0
	v_mfma_f32_16x16x128_f8f6f4 v[106:109], v[18:25], v[50:57], 0
	v_mfma_f32_16x16x128_f8f6f4 v[98:101], v[26:33], v[50:57], 0
	v_mfma_f32_16x16x128_f8f6f4 v[78:81], v[18:25], v[42:49], 0
	v_mfma_f32_16x16x128_f8f6f4 v[74:77], v[26:33], v[42:49], 0
	v_mfma_f32_16x16x128_f8f6f4 v[70:73], v[18:25], v[34:41], 0
	v_mfma_f32_16x16x128_f8f6f4 v[66:69], v[26:33], v[34:41], 0
	v_mfma_f32_16x16x128_f8f6f4 v[118:121], v[2:9], v[58:65], 0
	v_mfma_f32_16x16x128_f8f6f4 v[114:117], v[10:17], v[58:65], 0
	v_mfma_f32_16x16x128_f8f6f4 v[90:93], v[2:9], v[50:57], 0
	v_mfma_f32_16x16x128_f8f6f4 v[82:85], v[10:17], v[50:57], 0
	v_mfma_f32_16x16x128_f8f6f4 v[102:105], v[2:9], v[42:49], 0
	v_mfma_f32_16x16x128_f8f6f4 v[110:113], v[10:17], v[42:49], 0
	v_mfma_f32_16x16x128_f8f6f4 v[86:89], v[2:9], v[34:41], 0
	v_mfma_f32_16x16x128_f8f6f4 v[94:97], v[10:17], v[34:41], 0
	s_branch .Lnz_P8b_back
